# attention softmax merge: reference max and exp offset updated only when the reference changes; 3 VALU fewer per key sub-block
# baseline (speedup 1.0000x reference)
; #define LAS __attribute__((address_space(3)))
; DI unsigned pk2(float lo, float hi) { f32x2 v = {lo, hi}; return __builtin_bit_cast(unsigned, __builtin_convertvector(v, bf16v2)); }
;     ...
;                 mx = fmaxf(mx, __shfl_xor(mx, 32));
;                 const float mnew = fmaxf(mrun, mx); const bool grew = __any(mnew > mrun);
;                 if (grew) {
;                     const float alpha = __builtin_amdgcn_exp2f((mrun - mnew) * L2E);
;                     ls0 *= alpha; ls1 *= alpha; ls2 *= alpha; ls3 *= alpha;
; #pragma unroll
;                     for (int i = 0; i < 16; ++i) { oacc[0][i] *= alpha; oacc[1][i] *= alpha; } }
;                 mrun = mnew;
;                 const float nm = -mnew * L2E;
; #pragma unroll
;                 for (int k2 = 0; k2 < 2; ++k2) { const int kt = 2 * ck + k2;
; #pragma unroll
;                     for (int i = 0; i < 16; i += 4) { const float p0 = __builtin_amdgcn_exp2f(__builtin_fmaf(sacc[k2][i], L2E, nm)), p1 = __builtin_amdgcn_exp2f(__builtin_fmaf(sacc[k2][i + 1], L2E, nm)),
;                                                                   p2 = __builtin_amdgcn_exp2f(__builtin_fmaf(sacc[k2][i + 2], L2E, nm)), p3 = __builtin_amdgcn_exp2f(__builtin_fmaf(sacc[k2][i + 3], L2E, nm));
;                         sacc[k2][i] = p0; sacc[k2][i + 1] = p1; sacc[k2][i + 2] = p2; sacc[k2][i + 3] = p3; ls0 += p0; ls1 += p1; ls2 += p2; ls3 += p3; }
; #pragma unroll
;                     for (int cc = 0; cc < 2; ++cc) {
;                         u32x4 pw; pw.x = pk2(sacc[k2][8 * cc], sacc[k2][8 * cc + 1]); pw.y = pk2(sacc[k2][8 * cc + 2], sacc[k2][8 * cc + 3]); pw.z = pk2(sacc[k2][8 * cc + 4], sacc[k2][8 * cc + 5]); pw.w = pk2(sacc[k2][8 * cc + 6], sacc[k2][8 * cc + 7]);
;                         const bf16x8 pf = __builtin_bit_cast(bf16x8, pw);
;                         const int key0 = 32 * kt + 16 * cc + 4 * half;
; #pragma unroll
;                         for (int dt = 0; dt < 2; ++dt) { const LAS unsigned char* vb = Vt + (32 * dt + qi) * VT_PITCH + key0 * 2;
;                             const u32x2 va = *(const LAS u32x2*)vb, vb2 = *(const LAS u32x2*)(vb + 16);
;                             u32x4 vw; vw.x = va.x; vw.y = va.y; vw.z = vb2.x; vw.w = vb2.y;
;                             oacc[dt] = __builtin_amdgcn_mfma_f32_32x32x16_bf16(__builtin_bit_cast(bf16x8, vw), pf, oacc[dt], 0, 0, 0); } } }
;             }
.LBB0_2233:
	v_mov_b32_e32 v32, v64
	v_add_f32_e32 v33, 0x41800000, v202
	s_nop 0
	v_permlane32_swap_b32_e32 v32, v64
	v_max3_f32 v32, v202, v64, v32
	s_cmp_eq_u32 s21, 0
	s_cbranch_scc1 .Lattn_newref
	v_cmp_gt_f32_e32 vcc, v32, v33
	s_cbranch_vccz .LBB0_2235
	v_cndmask_b32_e32 v32, v202, v32, vcc
	v_sub_f32_e32 v33, v202, v32
	v_mul_f32_e32 v33, 0x3fb8aa3b, v33
	v_exp_f32_e32 v34, v33
	s_nop 0
	v_mul_f32_e32 v30, v34, v30
	v_mul_f32_e32 v31, v34, v31
	v_mul_f32_e32 v28, v34, v28
	v_mul_f32_e32 v29, v34, v29
	v_mul_f32_e32 v26, v34, v26
	v_mul_f32_e32 v27, v34, v27
	v_mul_f32_e32 v24, v34, v24
	v_mul_f32_e32 v25, v34, v25
	v_mul_f32_e32 v22, v34, v22
	v_mul_f32_e32 v23, v34, v23
	v_mul_f32_e32 v20, v34, v20
	v_mul_f32_e32 v21, v34, v21
	v_mul_f32_e32 v18, v34, v18
	v_mul_f32_e32 v19, v34, v19
	v_mul_f32_e32 v16, v34, v16
	v_mul_f32_e32 v17, v34, v17
	v_mul_f32_e32 v14, v34, v14
	v_mul_f32_e32 v15, v34, v15
	v_mul_f32_e32 v12, v34, v12
	v_mul_f32_e32 v13, v34, v13
	v_mul_f32_e32 v10, v34, v10
	v_mul_f32_e32 v11, v34, v11
	v_mul_f32_e32 v8, v34, v8
	v_mul_f32_e32 v9, v34, v9
	v_mul_f32_e32 v6, v34, v6
	v_mul_f32_e32 v7, v34, v7
	v_mul_f32_e32 v4, v34, v4
	v_mul_f32_e32 v5, v34, v5
	v_mul_f32_e32 v2, v34, v2
	v_mul_f32_e32 v3, v34, v3
	v_mul_f32_e32 v0, v34, v0
	v_mul_f32_e32 v1, v34, v1
	v_mul_f32_e32 v120, v34, v120
	v_mul_f32_e32 v121, v34, v121
	v_mul_f32_e32 v118, v34, v118
	v_mul_f32_e32 v119, v34, v119
.Lattn_newref:
	v_mov_b32_e32 v202, v32
	v_mul_f32_e32 v229, 0xbfb8aa3b, v32
.LBB0_2235:
	v_fmamk_f32 v126, v126, 0x3fb8aa3b, v229
	v_fmamk_f32 v127, v127, 0x3fb8aa3b, v229
	v_fmamk_f32 v122, v122, 0x3fb8aa3b, v229
	v_fmamk_f32 v123, v123, 0x3fb8aa3b, v229
	v_exp_f32_e32 v63, v126
	v_fmamk_f32 v128, v128, 0x3fb8aa3b, v229
	v_fmamk_f32 v129, v129, 0x3fb8aa3b, v229
	v_exp_f32_e32 v62, v127
	v_fmamk_f32 v124, v124, 0x3fb8aa3b, v229
	v_fmamk_f32 v125, v125, 0x3fb8aa3b, v229
	v_exp_f32_e32 v61, v122
	v_exp_f32_e32 v60, v123
	v_exp_f32_e32 v123, v128
	v_exp_f32_e32 v122, v129
	v_fmamk_f32 v130, v130, 0x3fb8aa3b, v229
	v_fmamk_f32 v131, v131, 0x3fb8aa3b, v229
	v_exp_f32_e32 v35, v124
	v_exp_f32_e32 v34, v125
	v_exp_f32_e32 v125, v130
	v_exp_f32_e32 v124, v131
	v_fmamk_f32 v132, v132, 0x3fb8aa3b, v229
	v_fmamk_f32 v133, v133, 0x3fb8aa3b, v229
	v_fmamk_f32 v164, v164, 0x3fb8aa3b, v229
	v_fmamk_f32 v165, v165, 0x3fb8aa3b, v229
	v_exp_f32_e32 v127, v132
	v_exp_f32_e32 v126, v133
	v_exp_f32_e32 v133, v164
	v_exp_f32_e32 v132, v165
	v_fmamk_f32 v134, v134, 0x3fb8aa3b, v229
	v_fmamk_f32 v135, v135, 0x3fb8aa3b, v229
	v_fmamk_f32 v166, v166, 0x3fb8aa3b, v229
	v_fmamk_f32 v167, v167, 0x3fb8aa3b, v229
	v_exp_f32_e32 v129, v134
	v_exp_f32_e32 v128, v135
	v_exp_f32_e32 v135, v166
	v_exp_f32_e32 v134, v167
	v_fmamk_f32 v136, v136, 0x3fb8aa3b, v229
	v_fmamk_f32 v137, v137, 0x3fb8aa3b, v229
	v_fmamk_f32 v168, v168, 0x3fb8aa3b, v229
	v_fmamk_f32 v169, v169, 0x3fb8aa3b, v229
	v_exp_f32_e32 v131, v136
	v_exp_f32_e32 v130, v137
	v_exp_f32_e32 v137, v168
	v_exp_f32_e32 v136, v169
	v_fmamk_f32 v170, v170, 0x3fb8aa3b, v229
	v_fmamk_f32 v171, v171, 0x3fb8aa3b, v229
	v_fmamk_f32 v172, v172, 0x3fb8aa3b, v229
	v_fmamk_f32 v173, v173, 0x3fb8aa3b, v229
	v_exp_f32_e32 v165, v170
	v_exp_f32_e32 v164, v171
	v_add_u32_e32 v58, 0x4000, v216
	v_exp_f32_e32 v167, v172
	v_exp_f32_e32 v166, v173
	v_fmamk_f32 v174, v174, 0x3fb8aa3b, v229
	v_fmamk_f32 v175, v175, 0x3fb8aa3b, v229
	ds_read2_b64 v[36:39], v216 offset1:2
	ds_read2_b64 v[40:43], v216 offset0:4 offset1:6
	ds_read2_b64 v[44:47], v58 offset0:32 offset1:34
	ds_read2_b64 v[48:51], v58 offset0:36 offset1:38
	v_fmamk_f32 v138, v138, 0x3fb8aa3b, v229
	v_fmamk_f32 v139, v139, 0x3fb8aa3b, v229
	v_exp_f32_e32 v169, v174
	v_exp_f32_e32 v168, v175
	v_cvt_pk_bf16_f32 v52, v61, v60
	v_cvt_pk_bf16_f32 v53, v35, v34
	v_cvt_pk_bf16_f32 v54, v63, v62
	v_cvt_pk_bf16_f32 v55, v123, v122
	v_exp_f32_e32 v171, v138
	v_exp_f32_e32 v170, v139
	s_waitcnt lgkmcnt(3)
	v_mfma_f32_32x32x16_bf16 v[16:31], v[36:39], v[52:55], v[16:31]
	v_fmamk_f32 v140, v140, 0x3fb8aa3b, v229
	v_fmamk_f32 v141, v141, 0x3fb8aa3b, v229
	v_cvt_pk_bf16_f32 v36, v125, v124
	v_exp_f32_e32 v139, v140
	s_waitcnt lgkmcnt(1)
	v_mfma_f32_32x32x16_bf16 v[0:15], v[44:47], v[52:55], v[0:15]
	v_cvt_pk_bf16_f32 v38, v129, v128
	v_cvt_pk_bf16_f32 v37, v127, v126
	v_add_f32_e32 v60, v60, v120
	v_add_f32_e32 v61, v61, v121
	v_cvt_pk_bf16_f32 v39, v131, v130
	v_exp_f32_e32 v138, v141
	s_nop 0
	v_mfma_f32_32x32x16_bf16 v[16:31], v[40:43], v[36:39], v[16:31]
	ds_read2_b64 v[40:43], v216 offset0:8 offset1:10
	ds_read2_b64 v[44:47], v58 offset0:40 offset1:42
	ds_read2_b64 v[52:55], v216 offset0:12 offset1:14
	ds_read2_b64 v[56:59], v58 offset0:44 offset1:46
	v_add_f32_e32 v34, v34, v118
	v_add_f32_e32 v35, v35, v119
	v_add_f32_e32 v34, v122, v34
	v_add_f32_e32 v35, v123, v35
	s_sub_i32 s21, s21, 64
	v_add_f32_e32 v34, v126, v34
	v_add_f32_e32 v35, v127, v35
	s_add_i32 s22, s22, 64
	s_waitcnt lgkmcnt(4)
	v_mfma_f32_32x32x16_bf16 v[0:15], v[48:51], v[36:39], v[0:15]
	v_cvt_pk_bf16_f32 v37, v135, v134
	v_cvt_pk_bf16_f32 v36, v133, v132
	v_cvt_pk_bf16_f32 v38, v137, v136
	v_cvt_pk_bf16_f32 v39, v165, v164
	v_add_f32_e32 v34, v130, v34
	v_add_f32_e32 v35, v131, v35
	s_cmpk_eq_i32 s21, 0xff00
	s_waitcnt lgkmcnt(3)
	v_mfma_f32_32x32x16_bf16 v[16:31], v[40:43], v[36:39], v[16:31]
	v_add_f32_e32 v40, v62, v60
	v_add_f32_e32 v41, v63, v61
	v_add_f32_e32 v40, v124, v40
	v_add_f32_e32 v41, v125, v41
	v_add_f32_e32 v34, v134, v34
	v_add_f32_e32 v35, v135, v35
	v_add_f32_e32 v40, v128, v40
	v_add_f32_e32 v41, v129, v41
	v_add_f32_e32 v34, v164, v34
	v_add_f32_e32 v35, v165, v35
	v_add_f32_e32 v40, v132, v40
	v_add_f32_e32 v41, v133, v41
	s_waitcnt lgkmcnt(2)
	v_mfma_f32_32x32x16_bf16 v[0:15], v[44:47], v[36:39], v[0:15]
	v_cvt_pk_bf16_f32 v36, v167, v166
	v_add_f32_e32 v40, v136, v40
	v_add_f32_e32 v41, v137, v41
	v_cvt_pk_bf16_f32 v37, v169, v168
	v_add_f32_e32 v40, v166, v40
	v_add_f32_e32 v41, v167, v41
	v_cvt_pk_bf16_f32 v38, v171, v170
	v_cvt_pk_bf16_f32 v39, v139, v138
	v_add_f32_e32 v34, v168, v34
	v_add_f32_e32 v35, v169, v35
	v_add_f32_e32 v120, v170, v40
	v_add_f32_e32 v121, v171, v41
	s_waitcnt lgkmcnt(1)
	v_mfma_f32_32x32x16_bf16 v[16:31], v[52:55], v[36:39], v[16:31]
	v_add_f32_e32 v118, v138, v34
	v_add_f32_e32 v119, v139, v35
	v_add_u32_e32 v216, 0x80, v216
	v_add_u32_e32 v251, 0x2400, v251
	s_cselect_b64 s[6:7], -1, 0
	s_waitcnt lgkmcnt(0)
	v_mfma_f32_32x32x16_bf16 v[0:15], v[56:59], v[36:39], v[0:15]
	s_and_b64 vcc, exec, s[6:7]
	s_cbranch_vccnz .LBB0_2238
.LBB0_2236:
	s_add_i32 s6, s22, 0xffffff41
	v_cmp_le_i32_e32 vcc, s6, v250
	s_cbranch_vccnz .LBB0_2230
	s_branch .LBB0_2229

; DI unsigned pk2(float lo, float hi) { f32x2 v = {lo, hi}; return __builtin_bit_cast(unsigned, __builtin_convertvector(v, bf16v2)); }
;     ...
;             float lsum = (ls0 + ls1) + (ls2 + ls3);
; #pragma unroll
;             for (int kk = 0; kk < 4; ++kk) asm volatile("" : "+v"(qfn[kk]));
;             asm volatile("" : "+v"(enn));
;             const float mx = mrun;
;             lsum += __shfl_xor(lsum, 32);
;             const float inv = 1.0f / lsum;
;             if (valid) {
;                 int hf = half; asm volatile("" : "+v"(hf));
;                 bf16_t* op = PO + ((size_t)slot * T + tok) * CW + h * 64 + 4 * hf;
; #pragma unroll
;                 for (int dt = 0; dt < 2; ++dt)
; #pragma unroll
;                     for (int ig = 0; ig < 4; ++ig) { u32x2 w; w.x = pk2(oacc[dt][4 * ig] * inv, oacc[dt][4 * ig + 1] * inv); w.y = pk2(oacc[dt][4 * ig + 2] * inv, oacc[dt][4 * ig + 3] * inv);
;                         *(u32x2*)(op + 32 * dt + 8 * ig) = w; }
;                 if (half == 0) PST[((size_t)slot * T + tok) * 8 + h] = (f32x2){mx, lsum};
;             }
.LBB0_2238:
	v_lshl_or_b32 v33, s20, 5, v149
	v_cmp_lt_i32_e32 vcc, v33, v245
	v_add_f32_e32 v33, v120, v121
	s_waitcnt lgkmcnt(0)
	v_add_f32_e32 v34, v118, v119
	v_add_f32_e32 v33, v34, v33
	s_nop 0
	v_mov_b32_e32 v34, v33
	s_nop 1
	v_permlane32_swap_b32_e32 v34, v33
	s_waitcnt vmcnt(3)
	s_waitcnt vmcnt(2)
	s_waitcnt vmcnt(1)
	s_waitcnt vmcnt(0)
	s_and_saveexec_b64 s[6:7], vcc
	s_cbranch_execz .LBB0_2225
	s_waitcnt lgkmcnt(0)
	v_add_f32_e32 v33, v33, v34
	v_div_scale_f32 v34, s[20:21], v33, v33, 1.0
	v_rcp_f32_e32 v35, v34
	v_div_scale_f32 v36, vcc, 1.0, v33, 1.0
	v_fma_f32 v37, -v34, v35, 1.0
	v_fmac_f32_e32 v35, v37, v35
	v_mul_f32_e32 v37, v36, v35
	v_fma_f32 v38, -v34, v37, v36
	v_fmac_f32_e32 v37, v38, v35
	v_fma_f32 v34, -v34, v37, v36
	v_mov_b32_e32 v36, 15
	v_lshlrev_b32_sdwa v36, v36, v248 dst_sel:DWORD dst_unused:UNUSED_PAD src0_sel:DWORD src1_sel:WORD_1
	v_div_fmas_f32 v34, v34, v35, v37
	v_mov_b32_e32 v35, v151
	v_add3_u32 v64, v249, s44, v36
	v_div_fixup_f32 v34, v34, v33, 1.0
	v_lshlrev_b64 v[36:37], 10, v[64:65]
	v_lshlrev_b32_e32 v38, 3, v35
	v_lshl_add_u64 v[36:37], s[0:1], 0, v[36:37]
	v_ashrrev_i32_e32 v39, 31, v38
	v_mul_f32_e32 v16, v34, v16
	v_mul_f32_e32 v17, v34, v17
	v_mul_f32_e32 v18, v34, v18
	v_mul_f32_e32 v19, v34, v19
	v_cvt_pk_bf16_f32 v16, v16, v17
	v_cvt_pk_bf16_f32 v17, v18, v19
	v_mul_f32_e32 v20, v34, v20
	v_mul_f32_e32 v21, v34, v21
	v_mul_f32_e32 v22, v34, v22
	v_mul_f32_e32 v23, v34, v23
	v_cvt_pk_bf16_f32 v18, v20, v21
	v_cvt_pk_bf16_f32 v19, v22, v23
	v_mul_f32_e32 v0, v34, v0
	v_mul_f32_e32 v1, v34, v1
	v_mul_f32_e32 v2, v34, v2
	v_mul_f32_e32 v3, v34, v3
	v_cvt_pk_bf16_f32 v0, v0, v1
	v_cvt_pk_bf16_f32 v1, v2, v3
	v_mul_f32_e32 v4, v34, v4
	v_mul_f32_e32 v5, v34, v5
	v_mul_f32_e32 v6, v34, v6
	v_mul_f32_e32 v7, v34, v7
	v_cvt_pk_bf16_f32 v2, v4, v5
	v_cvt_pk_bf16_f32 v3, v6, v7
	v_lshl_add_u64 v[36:37], v[38:39], 1, v[36:37]
	v_mul_f32_e32 v24, v34, v24
	v_mul_f32_e32 v25, v34, v25
	v_mul_f32_e32 v26, v34, v26
	v_mul_f32_e32 v27, v34, v27
	v_cvt_pk_bf16_f32 v24, v24, v25
	v_cvt_pk_bf16_f32 v25, v26, v27
	v_mul_f32_e32 v28, v34, v28
	v_mul_f32_e32 v29, v34, v29
	v_mul_f32_e32 v30, v34, v30
	v_mul_f32_e32 v31, v34, v31
	v_cvt_pk_bf16_f32 v26, v28, v29
	v_cvt_pk_bf16_f32 v27, v30, v31
	v_mul_f32_e32 v8, v34, v8
	v_mul_f32_e32 v9, v34, v9
	v_mul_f32_e32 v10, v34, v10
	v_mul_f32_e32 v11, v34, v11
	v_cvt_pk_bf16_f32 v8, v8, v9
	v_cvt_pk_bf16_f32 v9, v10, v11
	v_mul_f32_e32 v12, v34, v12
	v_mul_f32_e32 v13, v34, v13
	v_mul_f32_e32 v14, v34, v14
	v_mul_f32_e32 v15, v34, v15
	v_cvt_pk_bf16_f32 v10, v12, v13
	v_cvt_pk_bf16_f32 v11, v14, v15
	s_nop 1
	v_permlane32_swap_b32_e32 v16, v18
	v_permlane32_swap_b32_e32 v17, v19
	v_permlane32_swap_b32_e32 v0, v2
	v_permlane32_swap_b32_e32 v1, v3
	v_permlane32_swap_b32_e32 v24, v26
	v_permlane32_swap_b32_e32 v25, v27
	v_permlane32_swap_b32_e32 v8, v10
	v_permlane32_swap_b32_e32 v9, v11
	global_store_dwordx4 v[36:37], v[16:19], off
	global_store_dwordx4 v[36:37], v[0:3], off offset:64
	global_store_dwordx4 v[36:37], v[24:27], off offset:32
	global_store_dwordx4 v[36:37], v[8:11], off offset:96
	s_and_b64 exec, exec, s[12:13]
	s_cbranch_execz .LBB0_2225
	v_mov_b32_e32 v32, v202
	v_lshlrev_b64 v[0:1], 6, v[64:65]
	v_lshl_add_u64 v[0:1], s[2:3], 0, v[0:1]
	global_store_dwordx2 v[0:1], v[32:33], off
	s_branch .LBB0_2225
